# baseline (speedup 1.0000x reference)
_Z6gat_k1PKfS0_S0_S0_PDF16_S1_S1_Pf:
	s_load_dwordx8 s[4:11], s[0:1], 0x0
	s_load_dwordx8 s[12:19], s[0:1], 0x20
	v_lshrrev_b32_e32 v54, 6, v0
	v_bfe_u32 v123, v0, 4, 2
	v_and_b32_e32 v120, 15, v0
	v_lshlrev_b32_e32 v120, 4, v120
	v_lshl_or_b32 v120, v54, 8, v120
	v_mov_b32_e32 v121, 0
	v_and_b32_e32 v57, 0xc0, v0
	s_lshl_b32 s3, s2, 5
	v_and_b32_e32 v1, 63, v0
	v_bfe_u32 v55, v0, 5, 1
	v_lshlrev_b32_e32 v2, 8, v57
	v_mov_b32_e32 v19, 0
	v_or_b32_e32 v4, s3, v123
	v_and_b32_e32 v56, 31, v0
	v_lshl_or_b32 v18, v55, 11, v2
	v_lshlrev_b32_e32 v20, 4, v1
	v_mov_b32_e32 v21, v19
	v_ashrrev_i32_e32 v5, 31, v4
	s_waitcnt lgkmcnt(0)
	v_lshl_add_u64 v[2:3], s[6:7], 0, v[18:19]
	v_lshlrev_b32_e32 v18, 2, v56
	s_lshl_b32 s20, s3, 10
	s_add_u32 s20, s4, s20
	s_addc_u32 s21, s5, 0
	v_lshl_or_b32 v121, v123, 10, v120
	global_load_dwordx4 v[22:25], v121, s[20:21] nt
	s_add_u32 s20, s20, 0x1000
	s_addc_u32 s21, s21, 0
	global_load_dwordx4 v[26:29], v121, s[20:21] nt
	s_add_u32 s20, s20, 0x1000
	s_addc_u32 s21, s21, 0
	global_load_dwordx4 v[30:33], v121, s[20:21] nt
	s_add_u32 s20, s20, 0x1000
	s_addc_u32 s21, s21, 0
	global_load_dwordx4 v[34:37], v121, s[20:21] nt
	s_add_u32 s20, s20, 0x1000
	s_addc_u32 s21, s21, 0
	global_load_dwordx4 v[38:41], v121, s[20:21] nt
	s_add_u32 s20, s20, 0x1000
	s_addc_u32 s21, s21, 0
	global_load_dwordx4 v[42:45], v121, s[20:21] nt
	s_add_u32 s20, s20, 0x1000
	s_addc_u32 s21, s21, 0
	global_load_dwordx4 v[46:49], v121, s[20:21] nt
	s_add_u32 s20, s20, 0x1000
	s_addc_u32 s21, s21, 0
	global_load_dwordx4 v[50:53], v121, s[20:21] nt
	s_movk_i32 s4, 0x410
	v_mad_u32_u24 v122, v123, s4, v120
	v_lshl_add_u64 v[2:3], v[2:3], 0, v[18:19]
	v_lshl_add_u64 v[2:3], v[2:3], 0, v[18:19]
	s_movk_i32 s22, 0x1000
	s_mov_b32 s23, 0
	v_lshl_add_u64 v[4:5], v[2:3], 0, s[22:23]
	s_movk_i32 s22, 0x3000
	v_lshl_add_u64 v[6:7], v[2:3], 0, s[22:23]
	global_load_dwordx2 v[58:59], v[4:5], off offset:-4096
	global_load_dwordx2 v[60:61], v[4:5], off offset:-3840
	global_load_dwordx2 v[62:63], v[4:5], off offset:-3584
	global_load_dwordx2 v[64:65], v[4:5], off offset:-3328
	global_load_dwordx2 v[66:67], v[4:5], off offset:-3072
	global_load_dwordx2 v[68:69], v[4:5], off offset:-2816
	global_load_dwordx2 v[70:71], v[4:5], off offset:-2560
	global_load_dwordx2 v[72:73], v[4:5], off offset:-2304
	global_load_dwordx2 v[74:75], v[4:5], off
	global_load_dwordx2 v[76:77], v[4:5], off offset:256
	global_load_dwordx2 v[78:79], v[4:5], off offset:512
	global_load_dwordx2 v[80:81], v[4:5], off offset:768
	global_load_dwordx2 v[82:83], v[4:5], off offset:1024
	global_load_dwordx2 v[84:85], v[4:5], off offset:1280
	global_load_dwordx2 v[86:87], v[4:5], off offset:1536
	global_load_dwordx2 v[88:89], v[4:5], off offset:1792
	global_load_dwordx2 v[90:91], v[6:7], off offset:-4096
	global_load_dwordx2 v[92:93], v[6:7], off offset:-3840
	global_load_dwordx2 v[94:95], v[6:7], off offset:-3584
	global_load_dwordx2 v[96:97], v[6:7], off offset:-3328
	global_load_dwordx2 v[98:99], v[6:7], off offset:-3072
	global_load_dwordx2 v[100:101], v[6:7], off offset:-2816
	global_load_dwordx2 v[102:103], v[6:7], off offset:-2560
	global_load_dwordx2 v[104:105], v[6:7], off offset:-2304
	global_load_dwordx2 v[106:107], v[6:7], off
	global_load_dwordx2 v[108:109], v[6:7], off offset:256
	global_load_dwordx2 v[110:111], v[6:7], off offset:512
	global_load_dwordx2 v[112:113], v[6:7], off offset:768
	global_load_dwordx2 v[114:115], v[6:7], off offset:1024
	global_load_dwordx2 v[116:117], v[6:7], off offset:1280
	global_load_dwordx2 v[118:119], v[6:7], off offset:1536
	global_load_dwordx2 v[120:121], v[6:7], off offset:1792
	v_and_b32_e32 v1, 7, v0
	v_lshlrev_b32_e32 v123, 5, v1
	global_load_dwordx4 v[6:9], v123, s[8:9]
	global_load_dwordx4 v[2:5], v123, s[10:11]
	global_load_dwordx4 v[14:17], v123, s[8:9] offset:16
	global_load_dwordx4 v[10:13], v123, s[10:11] offset:16
	s_movk_i32 s8, 0x110
	s_waitcnt vmcnt(36)
	ds_write_b128 v122, v[22:25] offset:34816
	ds_write_b128 v122, v[26:29] offset:38976
	ds_write_b128 v122, v[30:33] offset:43136
	ds_write_b128 v122, v[34:37] offset:47296
	ds_write_b128 v122, v[38:41] offset:51456
	ds_write_b128 v122, v[42:45] offset:55616
	s_waitcnt vmcnt(36)
	ds_write_b128 v122, v[46:49] offset:59776
	s_waitcnt vmcnt(36)
	ds_write_b128 v122, v[50:53] offset:63936
	v_mul_u32_u24_e32 v22, 0x410, v56
	v_lshlrev_b32_e32 v23, 2, v57
	v_and_b32_e32 v24, 32, v0
	v_add3_u32 v38, v22, v23, v24
	s_waitcnt lgkmcnt(0)
	ds_read_b128 v[22:25], v38 offset:34832
	ds_read_b128 v[26:29], v38 offset:34816
	ds_read_b128 v[30:33], v38 offset:34880
	ds_read_b128 v[34:37], v38 offset:34896
	s_waitcnt lgkmcnt(3)
	v_cvt_pk_f16_f32 v25, v24, v25
	v_cvt_pk_f16_f32 v24, v22, v23
	s_waitcnt lgkmcnt(2)
	v_cvt_pk_f16_f32 v23, v28, v29
	v_cvt_pk_f16_f32 v22, v26, v27
	s_waitcnt vmcnt(28)
	v_cvt_pk_f16_f32 v29, v70, v72
	v_cvt_pk_f16_f32 v28, v66, v68
	v_cvt_pk_f16_f32 v27, v62, v64
	v_cvt_pk_f16_f32 v26, v58, v60
	v_lshlrev_b32_e32 v19, 2, v55
	s_nop 0
	v_mfma_f32_32x32x16_f16 a[0:15], v[22:25], v[26:29], 0
	s_waitcnt vmcnt(28)
	v_cvt_pk_f16_f32 v29, v71, v73
	v_cvt_pk_f16_f32 v28, v67, v69
	v_cvt_pk_f16_f32 v27, v63, v65
	v_cvt_pk_f16_f32 v26, v59, v61
	s_nop 1
	v_mfma_f32_32x32x16_f16 a[16:31], v[22:25], v[26:29], 0
	s_waitcnt lgkmcnt(0)
	v_cvt_pk_f16_f32 v25, v36, v37
	v_cvt_pk_f16_f32 v24, v34, v35
	v_cvt_pk_f16_f32 v23, v32, v33
	v_cvt_pk_f16_f32 v22, v30, v31
	ds_read_b128 v[30:33], v38 offset:34944
	ds_read_b128 v[34:37], v38 offset:34960
	s_waitcnt vmcnt(20)
	v_cvt_pk_f16_f32 v29, v86, v88
	v_cvt_pk_f16_f32 v28, v82, v84
	v_cvt_pk_f16_f32 v27, v78, v80
	s_waitcnt vmcnt(20)
	v_cvt_pk_f16_f32 v26, v74, v76
	s_nop 1
	v_mfma_f32_32x32x16_f16 a[0:15], v[22:25], v[26:29], a[0:15]
	v_cvt_pk_f16_f32 v29, v87, v89
	v_cvt_pk_f16_f32 v28, v83, v85
	v_cvt_pk_f16_f32 v27, v79, v81
	v_cvt_pk_f16_f32 v26, v75, v77
	s_nop 1
	v_mfma_f32_32x32x16_f16 a[16:31], v[22:25], v[26:29], a[16:31]
	s_waitcnt lgkmcnt(0)
	v_cvt_pk_f16_f32 v25, v36, v37
	v_cvt_pk_f16_f32 v24, v34, v35
	v_cvt_pk_f16_f32 v23, v32, v33
	v_cvt_pk_f16_f32 v22, v30, v31
	ds_read_b128 v[30:33], v38 offset:35008
	ds_read_b128 v[34:37], v38 offset:35024
	s_waitcnt vmcnt(12)
	v_cvt_pk_f16_f32 v29, v102, v104
	v_cvt_pk_f16_f32 v28, v98, v100
	v_cvt_pk_f16_f32 v27, v94, v96
	v_cvt_pk_f16_f32 v26, v90, v92
	s_nop 1
	v_mfma_f32_32x32x16_f16 a[0:15], v[22:25], v[26:29], a[0:15]
	s_waitcnt vmcnt(12)
	v_cvt_pk_f16_f32 v29, v103, v105
	v_cvt_pk_f16_f32 v28, v99, v101
	v_cvt_pk_f16_f32 v27, v95, v97
	v_cvt_pk_f16_f32 v26, v91, v93
	s_nop 1
	v_mfma_f32_32x32x16_f16 a[16:31], v[22:25], v[26:29], a[16:31]
	s_waitcnt lgkmcnt(0)
	v_cvt_pk_f16_f32 v25, v36, v37
	v_cvt_pk_f16_f32 v24, v34, v35
	v_cvt_pk_f16_f32 v23, v32, v33
	v_cvt_pk_f16_f32 v22, v30, v31
	s_waitcnt vmcnt(4)
	v_cvt_pk_f16_f32 v29, v118, v120
	v_cvt_pk_f16_f32 v28, v114, v116
	v_cvt_pk_f16_f32 v27, v110, v112
	v_cvt_pk_f16_f32 v26, v106, v108
	s_nop 1
	v_mfma_f32_32x32x16_f16 a[0:15], v[22:25], v[26:29], a[0:15]
	s_waitcnt vmcnt(4)
	v_cvt_pk_f16_f32 v29, v119, v121
	v_cvt_pk_f16_f32 v28, v115, v117
	v_cvt_pk_f16_f32 v27, v111, v113
	v_cvt_pk_f16_f32 v26, v107, v109
	s_nop 1
	v_mfma_f32_32x32x16_f16 a[16:31], v[22:25], v[26:29], a[16:31]
	v_lshl_or_b32 v22, v54, 5, v19
	v_mul_u32_u24_e32 v22, 0x44, v22
	v_lshl_add_u32 v22, v22, 2, v18
	v_add_u32_e32 v22, v22, v18
	v_add_u32_e32 v23, 0x880, v22
	v_add_u32_e32 v24, 0x1100, v22
	v_add_u32_e32 v25, 0x1980, v22
	s_nop 5
	ds_write2_b32 v22, a0, a16 offset1:1
	ds_write2_b32 v22, a1, a17 offset0:68 offset1:69
	ds_write2_b32 v22, a2, a18 offset0:136 offset1:137
	ds_write2_b32 v22, a3, a19 offset0:204 offset1:205
	ds_write2_b32 v23, a4, a20 offset1:1
	ds_write2_b32 v23, a5, a21 offset0:68 offset1:69
	ds_write2_b32 v23, a6, a22 offset0:136 offset1:137
	ds_write2_b32 v23, a7, a23 offset0:204 offset1:205
	ds_write2_b32 v24, a8, a24 offset1:1
	ds_write2_b32 v24, a9, a25 offset0:68 offset1:69
	ds_write2_b32 v24, a10, a26 offset0:136 offset1:137
	ds_write2_b32 v24, a11, a27 offset0:204 offset1:205
	ds_write2_b32 v25, a12, a28 offset1:1
	ds_write2_b32 v25, a13, a29 offset0:68 offset1:69
	ds_write2_b32 v25, a14, a30 offset0:136 offset1:137
	ds_write2_b32 v25, a15, a31 offset0:204 offset1:205
	v_lshrrev_b32_e32 v22, 3, v0
	v_mad_u32_u24 v23, v22, s8, v123
	s_waitcnt lgkmcnt(0)
	s_barrier
	ds_read_b128 v[24:27], v23
	ds_read_b128 v[28:31], v23 offset:16
	ds_read_b128 v[32:35], v23 offset:8704
	s_waitcnt lgkmcnt(2)
	v_pk_add_f32 v[36:37], v[26:27], 0 op_sel_hi:[1,0]
	v_pk_add_f32 v[38:39], v[24:25], 0 op_sel_hi:[1,0]
	ds_read_b128 v[24:27], v23 offset:8720
	s_waitcnt lgkmcnt(2)
	v_pk_add_f32 v[40:41], v[30:31], 0 op_sel_hi:[1,0]
	v_pk_add_f32 v[42:43], v[28:29], 0 op_sel_hi:[1,0]
	ds_read_b128 v[28:31], v23 offset:17408
	s_waitcnt lgkmcnt(2)
	v_pk_add_f32 v[34:35], v[36:37], v[34:35]
	v_pk_add_f32 v[36:37], v[38:39], v[32:33]
	s_waitcnt lgkmcnt(1)
	v_pk_add_f32 v[38:39], v[40:41], v[26:27]
	v_pk_add_f32 v[40:41], v[42:43], v[24:25]
	ds_read_b128 v[24:27], v23 offset:17424
	s_waitcnt lgkmcnt(1)
	v_pk_add_f32 v[42:43], v[34:35], v[30:31]
	ds_read_b128 v[30:33], v23 offset:26112
	v_pk_add_f32 v[28:29], v[36:37], v[28:29]
	ds_read_b128 v[34:37], v23 offset:26128
	s_waitcnt lgkmcnt(2)
	v_pk_add_f32 v[40:41], v[40:41], v[24:25]
	v_pk_add_f32 v[38:39], v[38:39], v[26:27]
	s_waitcnt lgkmcnt(1)
	v_pk_add_f32 v[24:25], v[28:29], v[30:31]
	v_pk_add_f32 v[26:27], v[42:43], v[32:33]
	s_waitcnt lgkmcnt(0)
	v_pk_add_f32 v[28:29], v[40:41], v[34:35]
	v_pk_add_f32 v[30:31], v[38:39], v[36:37]
	s_waitcnt vmcnt(0)
	v_mul_f32_e32 v10, v28, v10
	v_fmac_f32_e32 v10, v24, v2
	v_mul_f32_e32 v14, v28, v14
	v_add_f32_e32 v2, 0, v10
	v_mul_f32_e32 v10, v29, v15
	v_fmac_f32_e32 v14, v24, v6
	v_fmac_f32_e32 v10, v25, v7
	v_mul_f32_e32 v7, v29, v11
	v_add_f32_e32 v6, 0, v14
	v_fmac_f32_e32 v7, v25, v3
	v_mul_f32_e32 v3, v30, v16
	v_add_f32_e32 v6, v6, v10
	v_fmac_f32_e32 v3, v26, v8
	v_add_f32_e32 v3, v6, v3
	v_mul_f32_e32 v6, v30, v12
	v_fmac_f32_e32 v6, v26, v4
	v_mul_f32_e32 v4, v31, v17
	v_fmac_f32_e32 v4, v27, v9
	v_add_f32_e32 v2, v2, v7
	v_add_f32_e32 v3, v3, v4
	v_mul_f32_e32 v4, v31, v13
	v_add_f32_e32 v2, v2, v6
	v_fmac_f32_e32 v4, v27, v5
	v_add_f32_e32 v2, v2, v4
	ds_write_b128 v23, v[24:27]
	ds_write_b128 v23, v[28:31] offset:16
	s_nop 1
	v_add_f32_dpp v3, v3, v3 quad_perm:[1,0,3,2] row_mask:0xf bank_mask:0xf
	v_add_f32_dpp v6, v2, v2 quad_perm:[1,0,3,2] row_mask:0xf bank_mask:0xf
	s_nop 1
	v_add_f32_dpp v3, v3, v3 quad_perm:[2,3,0,1] row_mask:0xf bank_mask:0xf
	v_add_f32_dpp v6, v6, v6 quad_perm:[2,3,0,1] row_mask:0xf bank_mask:0xf
	s_nop 1
	v_add_f32_dpp v2, v3, v3 row_half_mirror row_mask:0xf bank_mask:0xf
	v_add_f32_dpp v3, v6, v6 row_half_mirror row_mask:0xf bank_mask:0xf
	v_cmp_eq_u32_e32 vcc, 0, v1
	s_and_saveexec_b64 s[6:7], vcc
	s_cbranch_execz .LBB0_2
	v_mul_f32_e32 v4, 0x3f7d70a4, v3
	v_mul_f32_e32 v4, 0x3fb8aa3b, v4
	v_mul_f32_e32 v3, 0x3c23d70a, v3
	v_exp_f32_e32 v4, v4
	v_mul_f32_e32 v3, 0x3fb8aa3b, v3
	v_exp_f32_e32 v3, v3
	v_lshlrev_b32_e32 v5, 2, v22
	v_or_b32_e32 v6, 0x10a80, v5
	v_mul_f32_e32 v2, 0xbf7d70a4, v2
	ds_write_b32 v6, v4
	v_or_b32_e32 v4, 0x10a00, v5
	v_mul_f32_e32 v2, 0x3fb8aa3b, v2
	ds_write_b32 v4, v3
	v_exp_f32_e32 v4, v2
	v_add_u32_e32 v2, s3, v22
	v_ashrrev_i32_e32 v3, 31, v2
	v_lshl_add_u64 v[2:3], v[2:3], 2, s[18:19]
	global_store_dword v[2:3], v4, off sc1
